# L1 prep key-block means: 16 loads in flight; shared-expert down epilogue: residual loads in 2 batches of 8
# speedup vs baseline: 1.0758x; 1.0047x over previous
; #define PG8_TILE_BEGIN(acc, wr, wc, fr, fq) \
;     _Pragma("unroll") for (int ai = 0; ai < 2; ++ai) _Pragma("unroll") for (int m = 0; m < 4; ++m) _Pragma("unroll") for (int bj = 0; bj < 2; ++bj) { \
;         const int trow = ai * 128 + wr * 64 + m * 16 + fr, tcol = bj * 128 + wc * 32 + 8 * fq; f32x4 v0 = acc[ai][bj][m][0], v1 = acc[ai][bj][m][1];
; __device__ __forceinline__ u32x4 pack8(f32x4 v0, f32x4 v1) { u32x4 w; w.x = cvt_pk_bf16(v0[0], v0[1]); w.y = cvt_pk_bf16(v0[2], v0[3]); w.z = cvt_pk_bf16(v1[0], v1[1]); w.w = cvt_pk_bf16(v1[2], v1[3]); return w; }
;     __device__ __forceinline__ void operator()(const f32x4 (&acc)[2][2][4][2], const pg8::Unit& u, int wr, int wc, int fr, int fq) const {
;         PG8_TILE_BEGIN(acc, wr, wc, fr, fq)
;             const size_t o_ = (size_t)(u.pm * 256 + trow) * ld + u.pn * 256 + tcol; const u32x4 r = *(const u32x4*)(R + o_);
;             v0[0] += scale * bflo(r.x); v0[1] += scale * bfhi(r.x); v0[2] += scale * bflo(r.y); v0[3] += scale * bfhi(r.y);
;             v1[0] += scale * bflo(r.z); v1[1] += scale * bfhi(r.z); v1[2] += scale * bflo(r.w); v1[3] += scale * bfhi(r.w);
;             *(u32x4*)(O + o_) = pg8::pack8(v0, v1);
.LBB0_2333:
	v_lshl_add_u32 v134, s54, 8, v215
	s_lshl_b32 s4, s16, 8
	v_readlane_b32 s18, v255, 13
	v_readlane_b32 s19, v255, 14
	v_lshlrev_b32_e32 v135, 11, v134
	v_or_b32_e32 v136, s4, v202
	v_or_b32_e32 v137, s4, v204
	v_lshl_add_u32 v136, v136, 1, v135
	v_lshl_add_u32 v137, v137, 1, v135
	v_readlane_b32 s20, v253, 46
	v_readlane_b32 s21, v253, 47
	s_and_b64 vcc, exec, s[0:1]
	s_mov_b64 s[4:5], -1
	v_mov_b32_e32 v138, v136
	global_load_dwordx4 v[138:141], v138, s[18:19]
	v_mov_b32_e32 v142, v137
	global_load_dwordx4 v[142:145], v142, s[18:19]
	v_add_u32_e32 v146, 0x8000, v136
	global_load_dwordx4 v[146:149], v146, s[18:19]
	v_add_u32_e32 v150, 0x8000, v137
	global_load_dwordx4 v[150:153], v150, s[18:19]
	v_add_u32_e32 v154, 0x10000, v136
	global_load_dwordx4 v[154:157], v154, s[18:19]
	v_add_u32_e32 v158, 0x10000, v137
	global_load_dwordx4 v[158:161], v158, s[18:19]
	v_add_u32_e32 v162, 0x18000, v136
	global_load_dwordx4 v[162:165], v162, s[18:19]
	v_add_u32_e32 v166, 0x18000, v137
	global_load_dwordx4 v[166:169], v166, s[18:19]
	s_waitcnt vmcnt(0)
	v_lshlrev_b32_e32 v170, 16, v138
	v_and_b32_e32 v171, 0xffff0000, v138
	v_lshlrev_b32_e32 v172, 16, v139
	v_and_b32_e32 v173, 0xffff0000, v139
	v_lshlrev_b32_e32 v174, 16, v140
	v_and_b32_e32 v175, 0xffff0000, v140
	v_lshlrev_b32_e32 v176, 16, v141
	v_and_b32_e32 v177, 0xffff0000, v141
	v_pk_fma_f32 v[130:131], v[170:171], s[10:11], v[130:131] op_sel_hi:[1,0,1]
	v_pk_fma_f32 v[132:133], v[172:173], s[10:11], v[132:133] op_sel_hi:[1,0,1]
	v_pk_fma_f32 v[126:127], v[174:175], s[10:11], v[126:127] op_sel_hi:[1,0,1]
	v_pk_fma_f32 v[128:129], v[176:177], s[10:11], v[128:129] op_sel_hi:[1,0,1]
	v_cvt_pk_bf16_f32 v138, v130, v131
	v_cvt_pk_bf16_f32 v139, v132, v133
	v_cvt_pk_bf16_f32 v140, v126, v127
	v_cvt_pk_bf16_f32 v141, v128, v129
	v_mov_b32_e32 v178, v136
	global_store_dwordx4 v178, v[138:141], s[20:21]
	v_lshlrev_b32_e32 v180, 16, v142
	v_and_b32_e32 v181, 0xffff0000, v142
	v_lshlrev_b32_e32 v182, 16, v143
	v_and_b32_e32 v183, 0xffff0000, v143
	v_lshlrev_b32_e32 v184, 16, v144
	v_and_b32_e32 v185, 0xffff0000, v144
	v_lshlrev_b32_e32 v186, 16, v145
	v_and_b32_e32 v187, 0xffff0000, v145
	v_pk_fma_f32 v[122:123], v[180:181], s[10:11], v[122:123] op_sel_hi:[1,0,1]
	v_pk_fma_f32 v[124:125], v[182:183], s[10:11], v[124:125] op_sel_hi:[1,0,1]
	v_pk_fma_f32 v[118:119], v[184:185], s[10:11], v[118:119] op_sel_hi:[1,0,1]
	v_pk_fma_f32 v[120:121], v[186:187], s[10:11], v[120:121] op_sel_hi:[1,0,1]
	v_cvt_pk_bf16_f32 v142, v122, v123
	v_cvt_pk_bf16_f32 v143, v124, v125
	v_cvt_pk_bf16_f32 v144, v118, v119
	v_cvt_pk_bf16_f32 v145, v120, v121
	v_mov_b32_e32 v188, v137
	global_store_dwordx4 v188, v[142:145], s[20:21]
	v_lshlrev_b32_e32 v170, 16, v146
	v_and_b32_e32 v171, 0xffff0000, v146
	v_lshlrev_b32_e32 v172, 16, v147
	v_and_b32_e32 v173, 0xffff0000, v147
	v_lshlrev_b32_e32 v174, 16, v148
	v_and_b32_e32 v175, 0xffff0000, v148
	v_lshlrev_b32_e32 v176, 16, v149
	v_and_b32_e32 v177, 0xffff0000, v149
	v_pk_fma_f32 v[114:115], v[170:171], s[10:11], v[114:115] op_sel_hi:[1,0,1]
	v_pk_fma_f32 v[116:117], v[172:173], s[10:11], v[116:117] op_sel_hi:[1,0,1]
	v_pk_fma_f32 v[110:111], v[174:175], s[10:11], v[110:111] op_sel_hi:[1,0,1]
	v_pk_fma_f32 v[112:113], v[176:177], s[10:11], v[112:113] op_sel_hi:[1,0,1]
	v_cvt_pk_bf16_f32 v146, v114, v115
	v_cvt_pk_bf16_f32 v147, v116, v117
	v_cvt_pk_bf16_f32 v148, v110, v111
	v_cvt_pk_bf16_f32 v149, v112, v113
	v_add_u32_e32 v178, 0x8000, v136
	global_store_dwordx4 v178, v[146:149], s[20:21]
	v_lshlrev_b32_e32 v180, 16, v150
	v_and_b32_e32 v181, 0xffff0000, v150
	v_lshlrev_b32_e32 v182, 16, v151
	v_and_b32_e32 v183, 0xffff0000, v151
	v_lshlrev_b32_e32 v184, 16, v152
	v_and_b32_e32 v185, 0xffff0000, v152
	v_lshlrev_b32_e32 v186, 16, v153
	v_and_b32_e32 v187, 0xffff0000, v153
	v_pk_fma_f32 v[106:107], v[180:181], s[10:11], v[106:107] op_sel_hi:[1,0,1]
	v_pk_fma_f32 v[108:109], v[182:183], s[10:11], v[108:109] op_sel_hi:[1,0,1]
	v_pk_fma_f32 v[102:103], v[184:185], s[10:11], v[102:103] op_sel_hi:[1,0,1]
	v_pk_fma_f32 v[104:105], v[186:187], s[10:11], v[104:105] op_sel_hi:[1,0,1]
	v_cvt_pk_bf16_f32 v150, v106, v107
	v_cvt_pk_bf16_f32 v151, v108, v109
	v_cvt_pk_bf16_f32 v152, v102, v103
	v_cvt_pk_bf16_f32 v153, v104, v105
	v_add_u32_e32 v188, 0x8000, v137
	global_store_dwordx4 v188, v[150:153], s[20:21]
	v_lshlrev_b32_e32 v170, 16, v154
	v_and_b32_e32 v171, 0xffff0000, v154
	v_lshlrev_b32_e32 v172, 16, v155
	v_and_b32_e32 v173, 0xffff0000, v155
	v_lshlrev_b32_e32 v174, 16, v156
	v_and_b32_e32 v175, 0xffff0000, v156
	v_lshlrev_b32_e32 v176, 16, v157
	v_and_b32_e32 v177, 0xffff0000, v157
	v_pk_fma_f32 v[98:99], v[170:171], s[10:11], v[98:99] op_sel_hi:[1,0,1]
	v_pk_fma_f32 v[100:101], v[172:173], s[10:11], v[100:101] op_sel_hi:[1,0,1]
	v_pk_fma_f32 v[94:95], v[174:175], s[10:11], v[94:95] op_sel_hi:[1,0,1]
	v_pk_fma_f32 v[96:97], v[176:177], s[10:11], v[96:97] op_sel_hi:[1,0,1]
	v_cvt_pk_bf16_f32 v154, v98, v99
	v_cvt_pk_bf16_f32 v155, v100, v101
	v_cvt_pk_bf16_f32 v156, v94, v95
	v_cvt_pk_bf16_f32 v157, v96, v97
	v_add_u32_e32 v178, 0x10000, v136
	global_store_dwordx4 v178, v[154:157], s[20:21]
	v_lshlrev_b32_e32 v180, 16, v158
	v_and_b32_e32 v181, 0xffff0000, v158
	v_lshlrev_b32_e32 v182, 16, v159
	v_and_b32_e32 v183, 0xffff0000, v159
	v_lshlrev_b32_e32 v184, 16, v160
	v_and_b32_e32 v185, 0xffff0000, v160
	v_lshlrev_b32_e32 v186, 16, v161
	v_and_b32_e32 v187, 0xffff0000, v161
	v_pk_fma_f32 v[90:91], v[180:181], s[10:11], v[90:91] op_sel_hi:[1,0,1]
	v_pk_fma_f32 v[92:93], v[182:183], s[10:11], v[92:93] op_sel_hi:[1,0,1]
	v_pk_fma_f32 v[86:87], v[184:185], s[10:11], v[86:87] op_sel_hi:[1,0,1]
; #define PG8_TILE_BEGIN(acc, wr, wc, fr, fq) \
;     _Pragma("unroll") for (int ai = 0; ai < 2; ++ai) _Pragma("unroll") for (int m = 0; m < 4; ++m) _Pragma("unroll") for (int bj = 0; bj < 2; ++bj) { \
;         const int trow = ai * 128 + wr * 64 + m * 16 + fr, tcol = bj * 128 + wc * 32 + 8 * fq; f32x4 v0 = acc[ai][bj][m][0], v1 = acc[ai][bj][m][1];
; __device__ __forceinline__ u32x4 pack8(f32x4 v0, f32x4 v1) { u32x4 w; w.x = cvt_pk_bf16(v0[0], v0[1]); w.y = cvt_pk_bf16(v0[2], v0[3]); w.z = cvt_pk_bf16(v1[0], v1[1]); w.w = cvt_pk_bf16(v1[2], v1[3]); return w; }
;     __device__ __forceinline__ void operator()(const f32x4 (&acc)[2][2][4][2], const pg8::Unit& u, int wr, int wc, int fr, int fq) const {
;         PG8_TILE_BEGIN(acc, wr, wc, fr, fq)
;             const size_t o_ = (size_t)(u.pm * 256 + trow) * ld + u.pn * 256 + tcol; const u32x4 r = *(const u32x4*)(R + o_);
;             v0[0] += scale * bflo(r.x); v0[1] += scale * bfhi(r.x); v0[2] += scale * bflo(r.y); v0[3] += scale * bfhi(r.y);
;             v1[0] += scale * bflo(r.z); v1[1] += scale * bfhi(r.z); v1[2] += scale * bflo(r.w); v1[3] += scale * bfhi(r.w);
;             *(u32x4*)(O + o_) = pg8::pack8(v0, v1);
	v_pk_fma_f32 v[88:89], v[186:187], s[10:11], v[88:89] op_sel_hi:[1,0,1]
	v_cvt_pk_bf16_f32 v158, v90, v91
	v_cvt_pk_bf16_f32 v159, v92, v93
	v_cvt_pk_bf16_f32 v160, v86, v87
	v_cvt_pk_bf16_f32 v161, v88, v89
	v_add_u32_e32 v188, 0x10000, v137
	global_store_dwordx4 v188, v[158:161], s[20:21]
	v_lshlrev_b32_e32 v170, 16, v162
	v_and_b32_e32 v171, 0xffff0000, v162
	v_lshlrev_b32_e32 v172, 16, v163
	v_and_b32_e32 v173, 0xffff0000, v163
	v_lshlrev_b32_e32 v174, 16, v164
	v_and_b32_e32 v175, 0xffff0000, v164
	v_lshlrev_b32_e32 v176, 16, v165
	v_and_b32_e32 v177, 0xffff0000, v165
	v_pk_fma_f32 v[82:83], v[170:171], s[10:11], v[82:83] op_sel_hi:[1,0,1]
	v_pk_fma_f32 v[84:85], v[172:173], s[10:11], v[84:85] op_sel_hi:[1,0,1]
	v_pk_fma_f32 v[78:79], v[174:175], s[10:11], v[78:79] op_sel_hi:[1,0,1]
	v_pk_fma_f32 v[80:81], v[176:177], s[10:11], v[80:81] op_sel_hi:[1,0,1]
	v_cvt_pk_bf16_f32 v162, v82, v83
	v_cvt_pk_bf16_f32 v163, v84, v85
	v_cvt_pk_bf16_f32 v164, v78, v79
	v_cvt_pk_bf16_f32 v165, v80, v81
	v_add_u32_e32 v178, 0x18000, v136
	global_store_dwordx4 v178, v[162:165], s[20:21]
	v_lshlrev_b32_e32 v180, 16, v166
	v_and_b32_e32 v181, 0xffff0000, v166
	v_lshlrev_b32_e32 v182, 16, v167
	v_and_b32_e32 v183, 0xffff0000, v167
	v_lshlrev_b32_e32 v184, 16, v168
	v_and_b32_e32 v185, 0xffff0000, v168
	v_lshlrev_b32_e32 v186, 16, v169
	v_and_b32_e32 v187, 0xffff0000, v169
	v_pk_fma_f32 v[74:75], v[180:181], s[10:11], v[74:75] op_sel_hi:[1,0,1]
	v_pk_fma_f32 v[76:77], v[182:183], s[10:11], v[76:77] op_sel_hi:[1,0,1]
	v_pk_fma_f32 v[70:71], v[184:185], s[10:11], v[70:71] op_sel_hi:[1,0,1]
	v_pk_fma_f32 v[72:73], v[186:187], s[10:11], v[72:73] op_sel_hi:[1,0,1]
	v_cvt_pk_bf16_f32 v166, v74, v75
	v_cvt_pk_bf16_f32 v167, v76, v77
	v_cvt_pk_bf16_f32 v168, v70, v71
	v_cvt_pk_bf16_f32 v169, v72, v73
	v_add_u32_e32 v188, 0x18000, v137
	global_store_dwordx4 v188, v[166:169], s[20:21]
	s_nop 1
	v_add_u32_e32 v138, 0x40000, v136
	global_load_dwordx4 v[138:141], v138, s[18:19]
	v_add_u32_e32 v142, 0x40000, v137
	global_load_dwordx4 v[142:145], v142, s[18:19]
	v_add_u32_e32 v146, 0x48000, v136
	global_load_dwordx4 v[146:149], v146, s[18:19]
	v_add_u32_e32 v150, 0x48000, v137
	global_load_dwordx4 v[150:153], v150, s[18:19]
	v_add_u32_e32 v154, 0x50000, v136
	global_load_dwordx4 v[154:157], v154, s[18:19]
	v_add_u32_e32 v158, 0x50000, v137
	global_load_dwordx4 v[158:161], v158, s[18:19]
	v_add_u32_e32 v162, 0x58000, v136
	global_load_dwordx4 v[162:165], v162, s[18:19]
	v_add_u32_e32 v166, 0x58000, v137
	global_load_dwordx4 v[166:169], v166, s[18:19]
	s_waitcnt vmcnt(0)
; #define PG8_TILE_BEGIN(acc, wr, wc, fr, fq) \
;     _Pragma("unroll") for (int ai = 0; ai < 2; ++ai) _Pragma("unroll") for (int m = 0; m < 4; ++m) _Pragma("unroll") for (int bj = 0; bj < 2; ++bj) { \
;         const int trow = ai * 128 + wr * 64 + m * 16 + fr, tcol = bj * 128 + wc * 32 + 8 * fq; f32x4 v0 = acc[ai][bj][m][0], v1 = acc[ai][bj][m][1];
; __device__ __forceinline__ u32x4 pack8(f32x4 v0, f32x4 v1) { u32x4 w; w.x = cvt_pk_bf16(v0[0], v0[1]); w.y = cvt_pk_bf16(v0[2], v0[3]); w.z = cvt_pk_bf16(v1[0], v1[1]); w.w = cvt_pk_bf16(v1[2], v1[3]); return w; }
;     __device__ __forceinline__ void operator()(const f32x4 (&acc)[2][2][4][2], const pg8::Unit& u, int wr, int wc, int fr, int fq) const {
;         PG8_TILE_BEGIN(acc, wr, wc, fr, fq)
;             const size_t o_ = (size_t)(u.pm * 256 + trow) * ld + u.pn * 256 + tcol; const u32x4 r = *(const u32x4*)(R + o_);
;             v0[0] += scale * bflo(r.x); v0[1] += scale * bfhi(r.x); v0[2] += scale * bflo(r.y); v0[3] += scale * bfhi(r.y);
;             v1[0] += scale * bflo(r.z); v1[1] += scale * bfhi(r.z); v1[2] += scale * bflo(r.w); v1[3] += scale * bfhi(r.w);
;             *(u32x4*)(O + o_) = pg8::pack8(v0, v1);
	v_lshlrev_b32_e32 v170, 16, v138
	v_and_b32_e32 v171, 0xffff0000, v138
	v_lshlrev_b32_e32 v172, 16, v139
	v_and_b32_e32 v173, 0xffff0000, v139
	v_lshlrev_b32_e32 v174, 16, v140
	v_and_b32_e32 v175, 0xffff0000, v140
	v_lshlrev_b32_e32 v176, 16, v141
	v_and_b32_e32 v177, 0xffff0000, v141
	v_pk_fma_f32 v[66:67], v[170:171], s[10:11], v[66:67] op_sel_hi:[1,0,1]
	v_pk_fma_f32 v[68:69], v[172:173], s[10:11], v[68:69] op_sel_hi:[1,0,1]
	v_pk_fma_f32 v[62:63], v[174:175], s[10:11], v[62:63] op_sel_hi:[1,0,1]
	v_pk_fma_f32 v[64:65], v[176:177], s[10:11], v[64:65] op_sel_hi:[1,0,1]
	v_cvt_pk_bf16_f32 v138, v66, v67
	v_cvt_pk_bf16_f32 v139, v68, v69
	v_cvt_pk_bf16_f32 v140, v62, v63
	v_cvt_pk_bf16_f32 v141, v64, v65
	v_add_u32_e32 v178, 0x40000, v136
	global_store_dwordx4 v178, v[138:141], s[20:21]
	v_lshlrev_b32_e32 v180, 16, v142
	v_and_b32_e32 v181, 0xffff0000, v142
	v_lshlrev_b32_e32 v182, 16, v143
	v_and_b32_e32 v183, 0xffff0000, v143
	v_lshlrev_b32_e32 v184, 16, v144
	v_and_b32_e32 v185, 0xffff0000, v144
	v_lshlrev_b32_e32 v186, 16, v145
	v_and_b32_e32 v187, 0xffff0000, v145
	v_pk_fma_f32 v[58:59], v[180:181], s[10:11], v[58:59] op_sel_hi:[1,0,1]
	v_pk_fma_f32 v[60:61], v[182:183], s[10:11], v[60:61] op_sel_hi:[1,0,1]
	v_pk_fma_f32 v[54:55], v[184:185], s[10:11], v[54:55] op_sel_hi:[1,0,1]
	v_pk_fma_f32 v[56:57], v[186:187], s[10:11], v[56:57] op_sel_hi:[1,0,1]
	v_cvt_pk_bf16_f32 v142, v58, v59
	v_cvt_pk_bf16_f32 v143, v60, v61
	v_cvt_pk_bf16_f32 v144, v54, v55
	v_cvt_pk_bf16_f32 v145, v56, v57
	v_add_u32_e32 v188, 0x40000, v137
	global_store_dwordx4 v188, v[142:145], s[20:21]
	v_lshlrev_b32_e32 v170, 16, v146
	v_and_b32_e32 v171, 0xffff0000, v146
	v_lshlrev_b32_e32 v172, 16, v147
	v_and_b32_e32 v173, 0xffff0000, v147
	v_lshlrev_b32_e32 v174, 16, v148
	v_and_b32_e32 v175, 0xffff0000, v148
	v_lshlrev_b32_e32 v176, 16, v149
	v_and_b32_e32 v177, 0xffff0000, v149
	v_pk_fma_f32 v[50:51], v[170:171], s[10:11], v[50:51] op_sel_hi:[1,0,1]
	v_pk_fma_f32 v[52:53], v[172:173], s[10:11], v[52:53] op_sel_hi:[1,0,1]
	v_pk_fma_f32 v[46:47], v[174:175], s[10:11], v[46:47] op_sel_hi:[1,0,1]
	v_pk_fma_f32 v[48:49], v[176:177], s[10:11], v[48:49] op_sel_hi:[1,0,1]
	v_cvt_pk_bf16_f32 v146, v50, v51
	v_cvt_pk_bf16_f32 v147, v52, v53
	v_cvt_pk_bf16_f32 v148, v46, v47
	v_cvt_pk_bf16_f32 v149, v48, v49
	v_add_u32_e32 v178, 0x48000, v136
	global_store_dwordx4 v178, v[146:149], s[20:21]
	v_lshlrev_b32_e32 v180, 16, v150
	v_and_b32_e32 v181, 0xffff0000, v150
	v_lshlrev_b32_e32 v182, 16, v151
	v_and_b32_e32 v183, 0xffff0000, v151
	v_lshlrev_b32_e32 v184, 16, v152
	v_and_b32_e32 v185, 0xffff0000, v152
	v_lshlrev_b32_e32 v186, 16, v153
	v_and_b32_e32 v187, 0xffff0000, v153
	v_pk_fma_f32 v[42:43], v[180:181], s[10:11], v[42:43] op_sel_hi:[1,0,1]
	v_pk_fma_f32 v[44:45], v[182:183], s[10:11], v[44:45] op_sel_hi:[1,0,1]
	v_pk_fma_f32 v[38:39], v[184:185], s[10:11], v[38:39] op_sel_hi:[1,0,1]
	v_pk_fma_f32 v[40:41], v[186:187], s[10:11], v[40:41] op_sel_hi:[1,0,1]
	v_cvt_pk_bf16_f32 v150, v42, v43
	v_cvt_pk_bf16_f32 v151, v44, v45
	v_cvt_pk_bf16_f32 v152, v38, v39
	v_cvt_pk_bf16_f32 v153, v40, v41
	v_add_u32_e32 v188, 0x48000, v137
	global_store_dwordx4 v188, v[150:153], s[20:21]
	v_lshlrev_b32_e32 v170, 16, v154
	v_and_b32_e32 v171, 0xffff0000, v154
	v_lshlrev_b32_e32 v172, 16, v155
	v_and_b32_e32 v173, 0xffff0000, v155
	v_lshlrev_b32_e32 v174, 16, v156
	v_and_b32_e32 v175, 0xffff0000, v156
	v_lshlrev_b32_e32 v176, 16, v157
	v_and_b32_e32 v177, 0xffff0000, v157
	v_pk_fma_f32 v[34:35], v[170:171], s[10:11], v[34:35] op_sel_hi:[1,0,1]
	v_pk_fma_f32 v[36:37], v[172:173], s[10:11], v[36:37] op_sel_hi:[1,0,1]
	v_pk_fma_f32 v[30:31], v[174:175], s[10:11], v[30:31] op_sel_hi:[1,0,1]
	v_pk_fma_f32 v[32:33], v[176:177], s[10:11], v[32:33] op_sel_hi:[1,0,1]
	v_cvt_pk_bf16_f32 v154, v34, v35
	v_cvt_pk_bf16_f32 v155, v36, v37
	v_cvt_pk_bf16_f32 v156, v30, v31
	v_cvt_pk_bf16_f32 v157, v32, v33
	v_add_u32_e32 v178, 0x50000, v136
	global_store_dwordx4 v178, v[154:157], s[20:21]
	v_lshlrev_b32_e32 v180, 16, v158
	v_and_b32_e32 v181, 0xffff0000, v158
	v_lshlrev_b32_e32 v182, 16, v159
	v_and_b32_e32 v183, 0xffff0000, v159
	v_lshlrev_b32_e32 v184, 16, v160
	v_and_b32_e32 v185, 0xffff0000, v160
	v_lshlrev_b32_e32 v186, 16, v161
	v_and_b32_e32 v187, 0xffff0000, v161
	v_pk_fma_f32 v[26:27], v[180:181], s[10:11], v[26:27] op_sel_hi:[1,0,1]
	v_pk_fma_f32 v[28:29], v[182:183], s[10:11], v[28:29] op_sel_hi:[1,0,1]
	v_pk_fma_f32 v[22:23], v[184:185], s[10:11], v[22:23] op_sel_hi:[1,0,1]
	v_pk_fma_f32 v[24:25], v[186:187], s[10:11], v[24:25] op_sel_hi:[1,0,1]
	v_cvt_pk_bf16_f32 v158, v26, v27
	v_cvt_pk_bf16_f32 v159, v28, v29
	v_cvt_pk_bf16_f32 v160, v22, v23
	v_cvt_pk_bf16_f32 v161, v24, v25
	v_add_u32_e32 v188, 0x50000, v137
	global_store_dwordx4 v188, v[158:161], s[20:21]
	v_lshlrev_b32_e32 v170, 16, v162
	v_and_b32_e32 v171, 0xffff0000, v162
	v_lshlrev_b32_e32 v172, 16, v163
	v_and_b32_e32 v173, 0xffff0000, v163
	v_lshlrev_b32_e32 v174, 16, v164
	v_and_b32_e32 v175, 0xffff0000, v164
	v_lshlrev_b32_e32 v176, 16, v165
	v_and_b32_e32 v177, 0xffff0000, v165
	v_pk_fma_f32 v[18:19], v[170:171], s[10:11], v[18:19] op_sel_hi:[1,0,1]
	v_pk_fma_f32 v[20:21], v[172:173], s[10:11], v[20:21] op_sel_hi:[1,0,1]
	v_pk_fma_f32 v[14:15], v[174:175], s[10:11], v[14:15] op_sel_hi:[1,0,1]
	v_pk_fma_f32 v[16:17], v[176:177], s[10:11], v[16:17] op_sel_hi:[1,0,1]
	v_cvt_pk_bf16_f32 v162, v18, v19
	v_cvt_pk_bf16_f32 v163, v20, v21
	v_cvt_pk_bf16_f32 v164, v14, v15
	v_cvt_pk_bf16_f32 v165, v16, v17
	v_add_u32_e32 v178, 0x58000, v136
	global_store_dwordx4 v178, v[162:165], s[20:21]
	v_lshlrev_b32_e32 v180, 16, v166
	v_and_b32_e32 v181, 0xffff0000, v166
	v_lshlrev_b32_e32 v182, 16, v167
	v_and_b32_e32 v183, 0xffff0000, v167
	v_lshlrev_b32_e32 v184, 16, v168
	v_and_b32_e32 v185, 0xffff0000, v168
	v_lshlrev_b32_e32 v186, 16, v169
	v_and_b32_e32 v187, 0xffff0000, v169
	v_pk_fma_f32 v[10:11], v[180:181], s[10:11], v[10:11] op_sel_hi:[1,0,1]
	v_pk_fma_f32 v[12:13], v[182:183], s[10:11], v[12:13] op_sel_hi:[1,0,1]
	v_pk_fma_f32 v[6:7], v[184:185], s[10:11], v[6:7] op_sel_hi:[1,0,1]
	v_pk_fma_f32 v[8:9], v[186:187], s[10:11], v[8:9] op_sel_hi:[1,0,1]
	v_cvt_pk_bf16_f32 v166, v10, v11
	v_cvt_pk_bf16_f32 v167, v12, v13
	v_cvt_pk_bf16_f32 v168, v6, v7
	v_cvt_pk_bf16_f32 v169, v8, v9
	v_add_u32_e32 v188, 0x58000, v137
	global_store_dwordx4 v188, v[166:169], s[20:21]
	s_cbranch_vccnz .LBB0_2308
	s_andn2_b64 vcc, exec, s[6:7]
	s_cbranch_vccnz .LBB0_2307
	s_barrier
	s_branch .LBB0_2307

; __device__ __forceinline__ void prep_phase(const Frame& F, const bf16_t* __restrict__ PROJ, const float* __restrict__ qn, const float* __restrict__ kvn, const f32x2* __restrict__ CS, bf16_t* __restrict__ CQN, bf16_t* __restrict__ CKVN, bf16_t* __restrict__ KB, float* __restrict__ KM) {
;     ...
;     for (int it = gw; it < NB * NBLK * HA; it += NGW) {
;         const int h = it % HA, blk = (it / HA) % NBLK, b = it / (HA * NBLK), c = lane & 7, r0 = lane >> 3;
;         const bf16_t* p = PROJ + ((size_t)b * SEQ + (size_t)blk * BLK + r0) * INCP + C_KA + h * 64 + c * 8;
;         float s[8];
; #pragma unroll
;         for (int i = 0; i < 8; ++i) s[i] = 0.f;
; #pragma unroll 16
;         for (int i = 0; i < 32; ++i) { const u32x4 v = *(const u32x4*)(p + (size_t)i * 8 * INCP);
; #pragma unroll
;             for (int k = 0; k < 4; ++k) { s[2 * k] += bflo(v[k]); s[2 * k + 1] += bfhi(v[k]); } }
; #pragma unroll
;         for (int i = 0; i < 8; ++i) { s[i] += __shfl_xor(s[i], 8); s[i] += __shfl_xor(s[i], 16); s[i] += __shfl_xor(s[i], 32); }
;         if (lane < 8) { float* o = KM + ((size_t)(b * HA + h) * NBLK + blk) * 64 + c * 8;
;             *(f32x4*)o = (f32x4){s[0], s[1], s[2], s[3]} * (1.f / BLK); *(f32x4*)(o + 4) = (f32x4){s[4], s[5], s[6], s[7]} * (1.f / BLK); }
.LBB0_2799:
	v_lshl_add_u64 v[18:19], v[8:9], 0, s[10:11]
	s_add_u32 s10, s10, 0x110000
	s_addc_u32 s11, s11, 0
	v_add_co_u32_e32 v100, vcc, 0x3b340000, v18
	s_nop 1
	v_addc_co_u32_e32 v101, vcc, 0, v19, vcc
	global_load_dwordx4 v[100:103], v[100:101], off offset:1024
	v_add_co_u32_e32 v104, vcc, 0x3b351000, v18
	s_nop 1
	v_addc_co_u32_e32 v105, vcc, 0, v19, vcc
	global_load_dwordx4 v[104:107], v[104:105], off offset:1024
	v_add_co_u32_e32 v108, vcc, 0x3b362000, v18
	s_nop 1
	v_addc_co_u32_e32 v109, vcc, 0, v19, vcc
	global_load_dwordx4 v[108:111], v[108:109], off offset:1024
	v_add_co_u32_e32 v112, vcc, 0x3b373000, v18
	s_nop 1
	v_addc_co_u32_e32 v113, vcc, 0, v19, vcc
	global_load_dwordx4 v[112:115], v[112:113], off offset:1024
	v_add_co_u32_e32 v116, vcc, 0x3b384000, v18
	s_nop 1
	v_addc_co_u32_e32 v117, vcc, 0, v19, vcc
	global_load_dwordx4 v[116:119], v[116:117], off offset:1024
	v_add_co_u32_e32 v120, vcc, 0x3b395000, v18
	s_nop 1
	v_addc_co_u32_e32 v121, vcc, 0, v19, vcc
	global_load_dwordx4 v[120:123], v[120:121], off offset:1024
	v_add_co_u32_e32 v124, vcc, 0x3b3a6000, v18
	s_nop 1
	v_addc_co_u32_e32 v125, vcc, 0, v19, vcc
	global_load_dwordx4 v[124:127], v[124:125], off offset:1024
	v_add_co_u32_e32 v128, vcc, 0x3b3b7000, v18
	s_nop 1
	v_addc_co_u32_e32 v129, vcc, 0, v19, vcc
	global_load_dwordx4 v[128:131], v[128:129], off offset:1024
	v_add_co_u32_e32 v132, vcc, 0x3b3c8000, v18
	s_nop 1
	v_addc_co_u32_e32 v133, vcc, 0, v19, vcc
	global_load_dwordx4 v[132:135], v[132:133], off offset:1024
	v_add_co_u32_e32 v136, vcc, 0x3b3d9000, v18
	s_nop 1
	v_addc_co_u32_e32 v137, vcc, 0, v19, vcc
	global_load_dwordx4 v[136:139], v[136:137], off offset:1024
	v_add_co_u32_e32 v140, vcc, 0x3b3ea000, v18
	s_nop 1
	v_addc_co_u32_e32 v141, vcc, 0, v19, vcc
	global_load_dwordx4 v[140:143], v[140:141], off offset:1024
	v_add_co_u32_e32 v144, vcc, 0x3b3fb000, v18
	s_nop 1
	v_addc_co_u32_e32 v145, vcc, 0, v19, vcc
	global_load_dwordx4 v[144:147], v[144:145], off offset:1024
	v_add_co_u32_e32 v148, vcc, 0x3b40c000, v18
	s_nop 1
	v_addc_co_u32_e32 v149, vcc, 0, v19, vcc
	global_load_dwordx4 v[148:151], v[148:149], off offset:1024
	v_add_co_u32_e32 v152, vcc, 0x3b41d000, v18
	s_nop 1
	v_addc_co_u32_e32 v153, vcc, 0, v19, vcc
	global_load_dwordx4 v[152:155], v[152:153], off offset:1024
	v_add_co_u32_e32 v156, vcc, 0x3b42e000, v18
	s_nop 1
	v_addc_co_u32_e32 v157, vcc, 0, v19, vcc
	global_load_dwordx4 v[156:159], v[156:157], off offset:1024
	v_add_co_u32_e32 v160, vcc, 0x3b43f000, v18
	s_nop 1
	v_addc_co_u32_e32 v161, vcc, 0, v19, vcc
	global_load_dwordx4 v[160:163], v[160:161], off offset:1024
	s_cmp_lg_u32 s10, 0x220000
	s_waitcnt vmcnt(15)
	v_lshlrev_b32_e32 v26, 16, v100
	v_and_b32_e32 v27, 0xffff0000, v100
	v_pk_add_f32 v[16:17], v[16:17], v[26:27]
	v_lshlrev_b32_e32 v20, 16, v101
	v_and_b32_e32 v21, 0xffff0000, v101
	v_pk_add_f32 v[14:15], v[14:15], v[20:21]
	v_lshlrev_b32_e32 v22, 16, v102
	v_and_b32_e32 v23, 0xffff0000, v102
	v_pk_add_f32 v[12:13], v[12:13], v[22:23]
	v_lshlrev_b32_e32 v26, 16, v103
	v_and_b32_e32 v27, 0xffff0000, v103
	v_pk_add_f32 v[10:11], v[10:11], v[26:27]
	s_waitcnt vmcnt(14)
	v_lshlrev_b32_e32 v26, 16, v104
	v_and_b32_e32 v27, 0xffff0000, v104
	v_pk_add_f32 v[16:17], v[16:17], v[26:27]
	v_lshlrev_b32_e32 v20, 16, v105
	v_and_b32_e32 v21, 0xffff0000, v105
	v_pk_add_f32 v[14:15], v[14:15], v[20:21]
	v_lshlrev_b32_e32 v22, 16, v106
	v_and_b32_e32 v23, 0xffff0000, v106
	v_pk_add_f32 v[12:13], v[12:13], v[22:23]
	v_lshlrev_b32_e32 v26, 16, v107
	v_and_b32_e32 v27, 0xffff0000, v107
	v_pk_add_f32 v[10:11], v[10:11], v[26:27]
	s_waitcnt vmcnt(13)
	v_lshlrev_b32_e32 v26, 16, v108
	v_and_b32_e32 v27, 0xffff0000, v108
	v_pk_add_f32 v[16:17], v[16:17], v[26:27]
	v_lshlrev_b32_e32 v20, 16, v109
	v_and_b32_e32 v21, 0xffff0000, v109
	v_pk_add_f32 v[14:15], v[14:15], v[20:21]
	v_lshlrev_b32_e32 v22, 16, v110
	v_and_b32_e32 v23, 0xffff0000, v110
	v_pk_add_f32 v[12:13], v[12:13], v[22:23]
	v_lshlrev_b32_e32 v26, 16, v111
	v_and_b32_e32 v27, 0xffff0000, v111
	v_pk_add_f32 v[10:11], v[10:11], v[26:27]
	s_waitcnt vmcnt(12)
	v_lshlrev_b32_e32 v26, 16, v112
	v_and_b32_e32 v27, 0xffff0000, v112
	v_pk_add_f32 v[16:17], v[16:17], v[26:27]
	v_lshlrev_b32_e32 v20, 16, v113
	v_and_b32_e32 v21, 0xffff0000, v113
	v_pk_add_f32 v[14:15], v[14:15], v[20:21]
	v_lshlrev_b32_e32 v22, 16, v114
	v_and_b32_e32 v23, 0xffff0000, v114
	v_pk_add_f32 v[12:13], v[12:13], v[22:23]
	v_lshlrev_b32_e32 v26, 16, v115
	v_and_b32_e32 v27, 0xffff0000, v115
	v_pk_add_f32 v[10:11], v[10:11], v[26:27]
	s_waitcnt vmcnt(11)
	v_lshlrev_b32_e32 v26, 16, v116
	v_and_b32_e32 v27, 0xffff0000, v116
	v_pk_add_f32 v[16:17], v[16:17], v[26:27]
	v_lshlrev_b32_e32 v20, 16, v117
	v_and_b32_e32 v21, 0xffff0000, v117
	v_pk_add_f32 v[14:15], v[14:15], v[20:21]
	v_lshlrev_b32_e32 v22, 16, v118
	v_and_b32_e32 v23, 0xffff0000, v118
	v_pk_add_f32 v[12:13], v[12:13], v[22:23]
	v_lshlrev_b32_e32 v26, 16, v119
	v_and_b32_e32 v27, 0xffff0000, v119
	v_pk_add_f32 v[10:11], v[10:11], v[26:27]
	s_waitcnt vmcnt(10)
	v_lshlrev_b32_e32 v26, 16, v120
	v_and_b32_e32 v27, 0xffff0000, v120
	v_pk_add_f32 v[16:17], v[16:17], v[26:27]
	v_lshlrev_b32_e32 v20, 16, v121
	v_and_b32_e32 v21, 0xffff0000, v121
	v_pk_add_f32 v[14:15], v[14:15], v[20:21]
	v_lshlrev_b32_e32 v22, 16, v122
	v_and_b32_e32 v23, 0xffff0000, v122
	v_pk_add_f32 v[12:13], v[12:13], v[22:23]
	v_lshlrev_b32_e32 v26, 16, v123
	v_and_b32_e32 v27, 0xffff0000, v123
	v_pk_add_f32 v[10:11], v[10:11], v[26:27]
	s_waitcnt vmcnt(9)
; __device__ __forceinline__ void prep_phase(const Frame& F, const bf16_t* __restrict__ PROJ, const float* __restrict__ qn, const float* __restrict__ kvn, const f32x2* __restrict__ CS, bf16_t* __restrict__ CQN, bf16_t* __restrict__ CKVN, bf16_t* __restrict__ KB, float* __restrict__ KM) {
;     ...
;     for (int it = gw; it < NB * NBLK * HA; it += NGW) {
;         const int h = it % HA, blk = (it / HA) % NBLK, b = it / (HA * NBLK), c = lane & 7, r0 = lane >> 3;
;         const bf16_t* p = PROJ + ((size_t)b * SEQ + (size_t)blk * BLK + r0) * INCP + C_KA + h * 64 + c * 8;
;         float s[8];
; #pragma unroll
;         for (int i = 0; i < 8; ++i) s[i] = 0.f;
; #pragma unroll 16
;         for (int i = 0; i < 32; ++i) { const u32x4 v = *(const u32x4*)(p + (size_t)i * 8 * INCP);
; #pragma unroll
;             for (int k = 0; k < 4; ++k) { s[2 * k] += bflo(v[k]); s[2 * k + 1] += bfhi(v[k]); } }
; #pragma unroll
;         for (int i = 0; i < 8; ++i) { s[i] += __shfl_xor(s[i], 8); s[i] += __shfl_xor(s[i], 16); s[i] += __shfl_xor(s[i], 32); }
;         if (lane < 8) { float* o = KM + ((size_t)(b * HA + h) * NBLK + blk) * 64 + c * 8;
;             *(f32x4*)o = (f32x4){s[0], s[1], s[2], s[3]} * (1.f / BLK); *(f32x4*)(o + 4) = (f32x4){s[4], s[5], s[6], s[7]} * (1.f / BLK); }
	v_lshlrev_b32_e32 v26, 16, v124
	v_and_b32_e32 v27, 0xffff0000, v124
	v_pk_add_f32 v[16:17], v[16:17], v[26:27]
	v_lshlrev_b32_e32 v20, 16, v125
	v_and_b32_e32 v21, 0xffff0000, v125
	v_pk_add_f32 v[14:15], v[14:15], v[20:21]
	v_lshlrev_b32_e32 v22, 16, v126
	v_and_b32_e32 v23, 0xffff0000, v126
	v_pk_add_f32 v[12:13], v[12:13], v[22:23]
	v_lshlrev_b32_e32 v26, 16, v127
	v_and_b32_e32 v27, 0xffff0000, v127
	v_pk_add_f32 v[10:11], v[10:11], v[26:27]
	s_waitcnt vmcnt(8)
	v_lshlrev_b32_e32 v26, 16, v128
	v_and_b32_e32 v27, 0xffff0000, v128
	v_pk_add_f32 v[16:17], v[16:17], v[26:27]
	v_lshlrev_b32_e32 v20, 16, v129
	v_and_b32_e32 v21, 0xffff0000, v129
	v_pk_add_f32 v[14:15], v[14:15], v[20:21]
	v_lshlrev_b32_e32 v22, 16, v130
	v_and_b32_e32 v23, 0xffff0000, v130
	v_pk_add_f32 v[12:13], v[12:13], v[22:23]
	v_lshlrev_b32_e32 v26, 16, v131
	v_and_b32_e32 v27, 0xffff0000, v131
	v_pk_add_f32 v[10:11], v[10:11], v[26:27]
	s_waitcnt vmcnt(7)
	v_lshlrev_b32_e32 v26, 16, v132
	v_and_b32_e32 v27, 0xffff0000, v132
	v_pk_add_f32 v[16:17], v[16:17], v[26:27]
	v_lshlrev_b32_e32 v20, 16, v133
	v_and_b32_e32 v21, 0xffff0000, v133
	v_pk_add_f32 v[14:15], v[14:15], v[20:21]
	v_lshlrev_b32_e32 v22, 16, v134
	v_and_b32_e32 v23, 0xffff0000, v134
	v_pk_add_f32 v[12:13], v[12:13], v[22:23]
	v_lshlrev_b32_e32 v26, 16, v135
	v_and_b32_e32 v27, 0xffff0000, v135
	v_pk_add_f32 v[10:11], v[10:11], v[26:27]
	s_waitcnt vmcnt(6)
	v_lshlrev_b32_e32 v26, 16, v136
	v_and_b32_e32 v27, 0xffff0000, v136
	v_pk_add_f32 v[16:17], v[16:17], v[26:27]
	v_lshlrev_b32_e32 v20, 16, v137
	v_and_b32_e32 v21, 0xffff0000, v137
	v_pk_add_f32 v[14:15], v[14:15], v[20:21]
	v_lshlrev_b32_e32 v22, 16, v138
	v_and_b32_e32 v23, 0xffff0000, v138
	v_pk_add_f32 v[12:13], v[12:13], v[22:23]
	v_lshlrev_b32_e32 v26, 16, v139
	v_and_b32_e32 v27, 0xffff0000, v139
	v_pk_add_f32 v[10:11], v[10:11], v[26:27]
	s_waitcnt vmcnt(5)
	v_lshlrev_b32_e32 v26, 16, v140
	v_and_b32_e32 v27, 0xffff0000, v140
	v_pk_add_f32 v[16:17], v[16:17], v[26:27]
	v_lshlrev_b32_e32 v20, 16, v141
	v_and_b32_e32 v21, 0xffff0000, v141
	v_pk_add_f32 v[14:15], v[14:15], v[20:21]
	v_lshlrev_b32_e32 v22, 16, v142
	v_and_b32_e32 v23, 0xffff0000, v142
	v_pk_add_f32 v[12:13], v[12:13], v[22:23]
	v_lshlrev_b32_e32 v26, 16, v143
	v_and_b32_e32 v27, 0xffff0000, v143
	v_pk_add_f32 v[10:11], v[10:11], v[26:27]
	s_waitcnt vmcnt(4)
	v_lshlrev_b32_e32 v26, 16, v144
	v_and_b32_e32 v27, 0xffff0000, v144
	v_pk_add_f32 v[16:17], v[16:17], v[26:27]
	v_lshlrev_b32_e32 v20, 16, v145
	v_and_b32_e32 v21, 0xffff0000, v145
	v_pk_add_f32 v[14:15], v[14:15], v[20:21]
	v_lshlrev_b32_e32 v22, 16, v146
	v_and_b32_e32 v23, 0xffff0000, v146
	v_pk_add_f32 v[12:13], v[12:13], v[22:23]
	v_lshlrev_b32_e32 v26, 16, v147
	v_and_b32_e32 v27, 0xffff0000, v147
	v_pk_add_f32 v[10:11], v[10:11], v[26:27]
	s_waitcnt vmcnt(3)
	v_lshlrev_b32_e32 v26, 16, v148
	v_and_b32_e32 v27, 0xffff0000, v148
	v_pk_add_f32 v[16:17], v[16:17], v[26:27]
	v_lshlrev_b32_e32 v20, 16, v149
	v_and_b32_e32 v21, 0xffff0000, v149
	v_pk_add_f32 v[14:15], v[14:15], v[20:21]
	v_lshlrev_b32_e32 v22, 16, v150
	v_and_b32_e32 v23, 0xffff0000, v150
	v_pk_add_f32 v[12:13], v[12:13], v[22:23]
	v_lshlrev_b32_e32 v26, 16, v151
	v_and_b32_e32 v27, 0xffff0000, v151
	v_pk_add_f32 v[10:11], v[10:11], v[26:27]
	s_waitcnt vmcnt(2)
	v_lshlrev_b32_e32 v26, 16, v152
	v_and_b32_e32 v27, 0xffff0000, v152
	v_pk_add_f32 v[16:17], v[16:17], v[26:27]
	v_lshlrev_b32_e32 v20, 16, v153
	v_and_b32_e32 v21, 0xffff0000, v153
	v_pk_add_f32 v[14:15], v[14:15], v[20:21]
	v_lshlrev_b32_e32 v22, 16, v154
	v_and_b32_e32 v23, 0xffff0000, v154
	v_pk_add_f32 v[12:13], v[12:13], v[22:23]
	v_lshlrev_b32_e32 v26, 16, v155
	v_and_b32_e32 v27, 0xffff0000, v155
	v_pk_add_f32 v[10:11], v[10:11], v[26:27]
	s_waitcnt vmcnt(1)
	v_lshlrev_b32_e32 v26, 16, v156
	v_and_b32_e32 v27, 0xffff0000, v156
	v_pk_add_f32 v[16:17], v[16:17], v[26:27]
	v_lshlrev_b32_e32 v20, 16, v157
	v_and_b32_e32 v21, 0xffff0000, v157
	v_pk_add_f32 v[14:15], v[14:15], v[20:21]
	v_lshlrev_b32_e32 v22, 16, v158
	v_and_b32_e32 v23, 0xffff0000, v158
	v_pk_add_f32 v[12:13], v[12:13], v[22:23]
	v_lshlrev_b32_e32 v26, 16, v159
	v_and_b32_e32 v27, 0xffff0000, v159
	v_pk_add_f32 v[10:11], v[10:11], v[26:27]
	s_waitcnt vmcnt(0)
	v_lshlrev_b32_e32 v26, 16, v160
	v_and_b32_e32 v27, 0xffff0000, v160
	v_pk_add_f32 v[16:17], v[16:17], v[26:27]
	v_lshlrev_b32_e32 v20, 16, v161
	v_and_b32_e32 v21, 0xffff0000, v161
	v_pk_add_f32 v[14:15], v[14:15], v[20:21]
	v_lshlrev_b32_e32 v22, 16, v162
	v_and_b32_e32 v23, 0xffff0000, v162
	v_pk_add_f32 v[12:13], v[12:13], v[22:23]
	v_lshlrev_b32_e32 v18, 16, v163
	v_and_b32_e32 v19, 0xffff0000, v163
	v_pk_add_f32 v[10:11], v[10:11], v[18:19]
	s_cbranch_scc1 .LBB0_2799
	ds_bpermute_b32 v8, v1, v16
	ds_bpermute_b32 v9, v1, v17
	ds_bpermute_b32 v18, v1, v14
	ds_bpermute_b32 v19, v1, v15
	ds_bpermute_b32 v22, v1, v12
	ds_bpermute_b32 v23, v1, v13
	s_waitcnt lgkmcnt(0)
	v_pk_add_f32 v[8:9], v[16:17], v[8:9]
	ds_bpermute_b32 v16, v24, v8
	v_pk_add_f32 v[18:19], v[14:15], v[18:19]
	ds_bpermute_b32 v17, v24, v9
	ds_bpermute_b32 v20, v24, v18
	ds_bpermute_b32 v21, v24, v19
	v_pk_add_f32 v[12:13], v[12:13], v[22:23]
	ds_bpermute_b32 v22, v24, v12
	s_waitcnt lgkmcnt(3)
	v_pk_add_f32 v[8:9], v[8:9], v[16:17]
	ds_bpermute_b32 v23, v24, v13
	s_waitcnt lgkmcnt(2)
	v_pk_add_f32 v[16:17], v[18:19], v[20:21]
	ds_bpermute_b32 v20, v1, v10
	ds_bpermute_b32 v21, v1, v11
	ds_bpermute_b32 v14, v25, v8
	ds_bpermute_b32 v15, v25, v9
	ds_bpermute_b32 v18, v25, v16
	ds_bpermute_b32 v19, v25, v17
	s_waitcnt lgkmcnt(4)
	v_pk_add_f32 v[20:21], v[10:11], v[20:21]
	ds_bpermute_b32 v26, v24, v20
	ds_bpermute_b32 v27, v24, v21
	v_pk_add_f32 v[10:11], v[12:13], v[22:23]
	ds_bpermute_b32 v12, v25, v10
	ds_bpermute_b32 v13, v25, v11
	s_waitcnt lgkmcnt(2)
	v_pk_add_f32 v[20:21], v[20:21], v[26:27]
	ds_bpermute_b32 v22, v25, v20
	ds_bpermute_b32 v23, v25, v21
	s_and_saveexec_b64 s[10:11], s[0:1]
	s_cbranch_execz .LBB0_2797
	s_lshl_b32 s8, s8, 3
	s_add_i32 s8, s8, s13
	s_ashr_i32 s9, s8, 31
	s_lshl_b64 s[8:9], s[8:9], 13
	v_readlane_b32 s14, v253, 62
	v_readlane_b32 s15, v253, 63
	s_add_u32 s8, s14, s8
	s_addc_u32 s9, s15, s9
	v_pk_add_f32 v[8:9], v[8:9], v[14:15]
	v_pk_add_f32 v[14:15], v[16:17], v[18:19]
	s_add_u32 s6, s8, s6
	s_waitcnt lgkmcnt(2)
	v_pk_add_f32 v[12:13], v[10:11], v[12:13]
	s_waitcnt lgkmcnt(0)
	v_pk_add_f32 v[16:17], v[20:21], v[22:23]
	s_addc_u32 s7, s9, s7
	v_pk_mul_f32 v[10:11], v[14:15], s[4:5] op_sel_hi:[1,0]
	v_pk_mul_f32 v[8:9], v[8:9], s[4:5] op_sel_hi:[1,0]
	global_store_dwordx4 v4, v[8:11], s[6:7]
	s_nop 1
	v_pk_mul_f32 v[10:11], v[16:17], s[4:5] op_sel_hi:[1,0]
	v_pk_mul_f32 v[8:9], v[12:13], s[4:5] op_sel_hi:[1,0]
	global_store_dwordx4 v4, v[8:11], s[6:7] offset:16
	s_branch .LBB0_2797

; #define PG8_TILE_BEGIN(acc, wr, wc, fr, fq) \
;     _Pragma("unroll") for (int ai = 0; ai < 2; ++ai) _Pragma("unroll") for (int m = 0; m < 4; ++m) _Pragma("unroll") for (int bj = 0; bj < 2; ++bj) { \
;         const int trow = ai * 128 + wr * 64 + m * 16 + fr, tcol = bj * 128 + wc * 32 + 8 * fq; f32x4 v0 = acc[ai][bj][m][0], v1 = acc[ai][bj][m][1];
; __device__ __forceinline__ u32x4 pack8(f32x4 v0, f32x4 v1) { u32x4 w; w.x = cvt_pk_bf16(v0[0], v0[1]); w.y = cvt_pk_bf16(v0[2], v0[3]); w.z = cvt_pk_bf16(v1[0], v1[1]); w.w = cvt_pk_bf16(v1[2], v1[3]); return w; }
;     __device__ __forceinline__ void operator()(const f32x4 (&acc)[2][2][4][2], const pg8::Unit& u, int wr, int wc, int fr, int fq) const {
;         PG8_TILE_BEGIN(acc, wr, wc, fr, fq)
;             const size_t o_ = (size_t)(u.pm * 256 + trow) * ld + u.pn * 256 + tcol; const u32x4 r = *(const u32x4*)(R + o_);
;             v0[0] += scale * bflo(r.x); v0[1] += scale * bfhi(r.x); v0[2] += scale * bflo(r.y); v0[3] += scale * bfhi(r.y);
;             v1[0] += scale * bflo(r.z); v1[1] += scale * bfhi(r.z); v1[2] += scale * bflo(r.w); v1[3] += scale * bfhi(r.w);
;             *(u32x4*)(O + o_) = pg8::pack8(v0, v1);
.LBB0_4793:
	v_lshl_add_u32 v134, s56, 8, v215
	s_lshl_b32 s2, s18, 8
	v_readlane_b32 s20, v255, 13
	v_readlane_b32 s21, v255, 14
	v_lshlrev_b32_e32 v135, 11, v134
	v_or_b32_e32 v136, s2, v202
	v_or_b32_e32 v137, s2, v204
	v_lshl_add_u32 v136, v136, 1, v135
	v_lshl_add_u32 v137, v137, 1, v135
	v_readlane_b32 s2, v253, 46
	v_readlane_b32 s3, v253, 47
	s_and_b64 vcc, exec, s[0:1]
	s_mov_b64 s[0:1], -1
	v_mov_b32_e32 v138, v136
	global_load_dwordx4 v[138:141], v138, s[20:21]
	v_mov_b32_e32 v142, v137
	global_load_dwordx4 v[142:145], v142, s[20:21]
	v_add_u32_e32 v146, 0x8000, v136
	global_load_dwordx4 v[146:149], v146, s[20:21]
	v_add_u32_e32 v150, 0x8000, v137
	global_load_dwordx4 v[150:153], v150, s[20:21]
	v_add_u32_e32 v154, 0x10000, v136
	global_load_dwordx4 v[154:157], v154, s[20:21]
	v_add_u32_e32 v158, 0x10000, v137
	global_load_dwordx4 v[158:161], v158, s[20:21]
	v_add_u32_e32 v162, 0x18000, v136
	global_load_dwordx4 v[162:165], v162, s[20:21]
	v_add_u32_e32 v166, 0x18000, v137
	global_load_dwordx4 v[166:169], v166, s[20:21]
	s_waitcnt vmcnt(0)
	v_lshlrev_b32_e32 v170, 16, v138
	v_and_b32_e32 v171, 0xffff0000, v138
	v_lshlrev_b32_e32 v172, 16, v139
	v_and_b32_e32 v173, 0xffff0000, v139
	v_lshlrev_b32_e32 v174, 16, v140
	v_and_b32_e32 v175, 0xffff0000, v140
	v_lshlrev_b32_e32 v176, 16, v141
	v_and_b32_e32 v177, 0xffff0000, v141
	v_pk_fma_f32 v[130:131], v[170:171], s[10:11], v[130:131] op_sel_hi:[1,0,1]
	v_pk_fma_f32 v[132:133], v[172:173], s[10:11], v[132:133] op_sel_hi:[1,0,1]
	v_pk_fma_f32 v[126:127], v[174:175], s[10:11], v[126:127] op_sel_hi:[1,0,1]
	v_pk_fma_f32 v[128:129], v[176:177], s[10:11], v[128:129] op_sel_hi:[1,0,1]
	v_cvt_pk_bf16_f32 v138, v130, v131
	v_cvt_pk_bf16_f32 v139, v132, v133
	v_cvt_pk_bf16_f32 v140, v126, v127
	v_cvt_pk_bf16_f32 v141, v128, v129
	v_mov_b32_e32 v178, v136
	global_store_dwordx4 v178, v[138:141], s[2:3]
	v_lshlrev_b32_e32 v180, 16, v142
	v_and_b32_e32 v181, 0xffff0000, v142
	v_lshlrev_b32_e32 v182, 16, v143
	v_and_b32_e32 v183, 0xffff0000, v143
	v_lshlrev_b32_e32 v184, 16, v144
	v_and_b32_e32 v185, 0xffff0000, v144
	v_lshlrev_b32_e32 v186, 16, v145
	v_and_b32_e32 v187, 0xffff0000, v145
	v_pk_fma_f32 v[122:123], v[180:181], s[10:11], v[122:123] op_sel_hi:[1,0,1]
	v_pk_fma_f32 v[124:125], v[182:183], s[10:11], v[124:125] op_sel_hi:[1,0,1]
	v_pk_fma_f32 v[118:119], v[184:185], s[10:11], v[118:119] op_sel_hi:[1,0,1]
	v_pk_fma_f32 v[120:121], v[186:187], s[10:11], v[120:121] op_sel_hi:[1,0,1]
	v_cvt_pk_bf16_f32 v142, v122, v123
	v_cvt_pk_bf16_f32 v143, v124, v125
	v_cvt_pk_bf16_f32 v144, v118, v119
	v_cvt_pk_bf16_f32 v145, v120, v121
	v_mov_b32_e32 v188, v137
	global_store_dwordx4 v188, v[142:145], s[2:3]
	v_lshlrev_b32_e32 v170, 16, v146
	v_and_b32_e32 v171, 0xffff0000, v146
	v_lshlrev_b32_e32 v172, 16, v147
	v_and_b32_e32 v173, 0xffff0000, v147
	v_lshlrev_b32_e32 v174, 16, v148
	v_and_b32_e32 v175, 0xffff0000, v148
	v_lshlrev_b32_e32 v176, 16, v149
	v_and_b32_e32 v177, 0xffff0000, v149
	v_pk_fma_f32 v[114:115], v[170:171], s[10:11], v[114:115] op_sel_hi:[1,0,1]
	v_pk_fma_f32 v[116:117], v[172:173], s[10:11], v[116:117] op_sel_hi:[1,0,1]
	v_pk_fma_f32 v[110:111], v[174:175], s[10:11], v[110:111] op_sel_hi:[1,0,1]
	v_pk_fma_f32 v[112:113], v[176:177], s[10:11], v[112:113] op_sel_hi:[1,0,1]
	v_cvt_pk_bf16_f32 v146, v114, v115
	v_cvt_pk_bf16_f32 v147, v116, v117
	v_cvt_pk_bf16_f32 v148, v110, v111
	v_cvt_pk_bf16_f32 v149, v112, v113
	v_add_u32_e32 v178, 0x8000, v136
	global_store_dwordx4 v178, v[146:149], s[2:3]
	v_lshlrev_b32_e32 v180, 16, v150
	v_and_b32_e32 v181, 0xffff0000, v150
	v_lshlrev_b32_e32 v182, 16, v151
	v_and_b32_e32 v183, 0xffff0000, v151
	v_lshlrev_b32_e32 v184, 16, v152
	v_and_b32_e32 v185, 0xffff0000, v152
	v_lshlrev_b32_e32 v186, 16, v153
	v_and_b32_e32 v187, 0xffff0000, v153
	v_pk_fma_f32 v[106:107], v[180:181], s[10:11], v[106:107] op_sel_hi:[1,0,1]
	v_pk_fma_f32 v[108:109], v[182:183], s[10:11], v[108:109] op_sel_hi:[1,0,1]
	v_pk_fma_f32 v[102:103], v[184:185], s[10:11], v[102:103] op_sel_hi:[1,0,1]
	v_pk_fma_f32 v[104:105], v[186:187], s[10:11], v[104:105] op_sel_hi:[1,0,1]
	v_cvt_pk_bf16_f32 v150, v106, v107
	v_cvt_pk_bf16_f32 v151, v108, v109
	v_cvt_pk_bf16_f32 v152, v102, v103
	v_cvt_pk_bf16_f32 v153, v104, v105
	v_add_u32_e32 v188, 0x8000, v137
	global_store_dwordx4 v188, v[150:153], s[2:3]
	v_lshlrev_b32_e32 v170, 16, v154
	v_and_b32_e32 v171, 0xffff0000, v154
	v_lshlrev_b32_e32 v172, 16, v155
	v_and_b32_e32 v173, 0xffff0000, v155
	v_lshlrev_b32_e32 v174, 16, v156
	v_and_b32_e32 v175, 0xffff0000, v156
	v_lshlrev_b32_e32 v176, 16, v157
	v_and_b32_e32 v177, 0xffff0000, v157
	v_pk_fma_f32 v[98:99], v[170:171], s[10:11], v[98:99] op_sel_hi:[1,0,1]
	v_pk_fma_f32 v[100:101], v[172:173], s[10:11], v[100:101] op_sel_hi:[1,0,1]
	v_pk_fma_f32 v[94:95], v[174:175], s[10:11], v[94:95] op_sel_hi:[1,0,1]
	v_pk_fma_f32 v[96:97], v[176:177], s[10:11], v[96:97] op_sel_hi:[1,0,1]
	v_cvt_pk_bf16_f32 v154, v98, v99
	v_cvt_pk_bf16_f32 v155, v100, v101
	v_cvt_pk_bf16_f32 v156, v94, v95
	v_cvt_pk_bf16_f32 v157, v96, v97
	v_add_u32_e32 v178, 0x10000, v136
	global_store_dwordx4 v178, v[154:157], s[2:3]
	v_lshlrev_b32_e32 v180, 16, v158
	v_and_b32_e32 v181, 0xffff0000, v158
	v_lshlrev_b32_e32 v182, 16, v159
	v_and_b32_e32 v183, 0xffff0000, v159
	v_lshlrev_b32_e32 v184, 16, v160
	v_and_b32_e32 v185, 0xffff0000, v160
	v_lshlrev_b32_e32 v186, 16, v161
	v_and_b32_e32 v187, 0xffff0000, v161
	v_pk_fma_f32 v[90:91], v[180:181], s[10:11], v[90:91] op_sel_hi:[1,0,1]
	v_pk_fma_f32 v[92:93], v[182:183], s[10:11], v[92:93] op_sel_hi:[1,0,1]
	v_pk_fma_f32 v[86:87], v[184:185], s[10:11], v[86:87] op_sel_hi:[1,0,1]
; #define PG8_TILE_BEGIN(acc, wr, wc, fr, fq) \
;     _Pragma("unroll") for (int ai = 0; ai < 2; ++ai) _Pragma("unroll") for (int m = 0; m < 4; ++m) _Pragma("unroll") for (int bj = 0; bj < 2; ++bj) { \
;         const int trow = ai * 128 + wr * 64 + m * 16 + fr, tcol = bj * 128 + wc * 32 + 8 * fq; f32x4 v0 = acc[ai][bj][m][0], v1 = acc[ai][bj][m][1];
; __device__ __forceinline__ u32x4 pack8(f32x4 v0, f32x4 v1) { u32x4 w; w.x = cvt_pk_bf16(v0[0], v0[1]); w.y = cvt_pk_bf16(v0[2], v0[3]); w.z = cvt_pk_bf16(v1[0], v1[1]); w.w = cvt_pk_bf16(v1[2], v1[3]); return w; }
;     __device__ __forceinline__ void operator()(const f32x4 (&acc)[2][2][4][2], const pg8::Unit& u, int wr, int wc, int fr, int fq) const {
;         PG8_TILE_BEGIN(acc, wr, wc, fr, fq)
;             const size_t o_ = (size_t)(u.pm * 256 + trow) * ld + u.pn * 256 + tcol; const u32x4 r = *(const u32x4*)(R + o_);
;             v0[0] += scale * bflo(r.x); v0[1] += scale * bfhi(r.x); v0[2] += scale * bflo(r.y); v0[3] += scale * bfhi(r.y);
;             v1[0] += scale * bflo(r.z); v1[1] += scale * bfhi(r.z); v1[2] += scale * bflo(r.w); v1[3] += scale * bfhi(r.w);
;             *(u32x4*)(O + o_) = pg8::pack8(v0, v1);
	v_pk_fma_f32 v[88:89], v[186:187], s[10:11], v[88:89] op_sel_hi:[1,0,1]
	v_cvt_pk_bf16_f32 v158, v90, v91
	v_cvt_pk_bf16_f32 v159, v92, v93
	v_cvt_pk_bf16_f32 v160, v86, v87
	v_cvt_pk_bf16_f32 v161, v88, v89
	v_add_u32_e32 v188, 0x10000, v137
	global_store_dwordx4 v188, v[158:161], s[2:3]
	v_lshlrev_b32_e32 v170, 16, v162
	v_and_b32_e32 v171, 0xffff0000, v162
	v_lshlrev_b32_e32 v172, 16, v163
	v_and_b32_e32 v173, 0xffff0000, v163
	v_lshlrev_b32_e32 v174, 16, v164
	v_and_b32_e32 v175, 0xffff0000, v164
	v_lshlrev_b32_e32 v176, 16, v165
	v_and_b32_e32 v177, 0xffff0000, v165
	v_pk_fma_f32 v[82:83], v[170:171], s[10:11], v[82:83] op_sel_hi:[1,0,1]
	v_pk_fma_f32 v[84:85], v[172:173], s[10:11], v[84:85] op_sel_hi:[1,0,1]
	v_pk_fma_f32 v[78:79], v[174:175], s[10:11], v[78:79] op_sel_hi:[1,0,1]
	v_pk_fma_f32 v[80:81], v[176:177], s[10:11], v[80:81] op_sel_hi:[1,0,1]
	v_cvt_pk_bf16_f32 v162, v82, v83
	v_cvt_pk_bf16_f32 v163, v84, v85
	v_cvt_pk_bf16_f32 v164, v78, v79
	v_cvt_pk_bf16_f32 v165, v80, v81
	v_add_u32_e32 v178, 0x18000, v136
	global_store_dwordx4 v178, v[162:165], s[2:3]
	v_lshlrev_b32_e32 v180, 16, v166
	v_and_b32_e32 v181, 0xffff0000, v166
	v_lshlrev_b32_e32 v182, 16, v167
	v_and_b32_e32 v183, 0xffff0000, v167
	v_lshlrev_b32_e32 v184, 16, v168
	v_and_b32_e32 v185, 0xffff0000, v168
	v_lshlrev_b32_e32 v186, 16, v169
	v_and_b32_e32 v187, 0xffff0000, v169
	v_pk_fma_f32 v[74:75], v[180:181], s[10:11], v[74:75] op_sel_hi:[1,0,1]
	v_pk_fma_f32 v[76:77], v[182:183], s[10:11], v[76:77] op_sel_hi:[1,0,1]
	v_pk_fma_f32 v[70:71], v[184:185], s[10:11], v[70:71] op_sel_hi:[1,0,1]
	v_pk_fma_f32 v[72:73], v[186:187], s[10:11], v[72:73] op_sel_hi:[1,0,1]
	v_cvt_pk_bf16_f32 v166, v74, v75
	v_cvt_pk_bf16_f32 v167, v76, v77
	v_cvt_pk_bf16_f32 v168, v70, v71
	v_cvt_pk_bf16_f32 v169, v72, v73
	v_add_u32_e32 v188, 0x18000, v137
	global_store_dwordx4 v188, v[166:169], s[2:3]
	s_nop 1
	v_add_u32_e32 v138, 0x40000, v136
	global_load_dwordx4 v[138:141], v138, s[20:21]
	v_add_u32_e32 v142, 0x40000, v137
	global_load_dwordx4 v[142:145], v142, s[20:21]
	v_add_u32_e32 v146, 0x48000, v136
	global_load_dwordx4 v[146:149], v146, s[20:21]
	v_add_u32_e32 v150, 0x48000, v137
	global_load_dwordx4 v[150:153], v150, s[20:21]
	v_add_u32_e32 v154, 0x50000, v136
	global_load_dwordx4 v[154:157], v154, s[20:21]
	v_add_u32_e32 v158, 0x50000, v137
	global_load_dwordx4 v[158:161], v158, s[20:21]
	v_add_u32_e32 v162, 0x58000, v136
	global_load_dwordx4 v[162:165], v162, s[20:21]
	v_add_u32_e32 v166, 0x58000, v137
	global_load_dwordx4 v[166:169], v166, s[20:21]
	s_waitcnt vmcnt(0)
; #define PG8_TILE_BEGIN(acc, wr, wc, fr, fq) \
;     _Pragma("unroll") for (int ai = 0; ai < 2; ++ai) _Pragma("unroll") for (int m = 0; m < 4; ++m) _Pragma("unroll") for (int bj = 0; bj < 2; ++bj) { \
;         const int trow = ai * 128 + wr * 64 + m * 16 + fr, tcol = bj * 128 + wc * 32 + 8 * fq; f32x4 v0 = acc[ai][bj][m][0], v1 = acc[ai][bj][m][1];
; __device__ __forceinline__ u32x4 pack8(f32x4 v0, f32x4 v1) { u32x4 w; w.x = cvt_pk_bf16(v0[0], v0[1]); w.y = cvt_pk_bf16(v0[2], v0[3]); w.z = cvt_pk_bf16(v1[0], v1[1]); w.w = cvt_pk_bf16(v1[2], v1[3]); return w; }
;     __device__ __forceinline__ void operator()(const f32x4 (&acc)[2][2][4][2], const pg8::Unit& u, int wr, int wc, int fr, int fq) const {
;         PG8_TILE_BEGIN(acc, wr, wc, fr, fq)
;             const size_t o_ = (size_t)(u.pm * 256 + trow) * ld + u.pn * 256 + tcol; const u32x4 r = *(const u32x4*)(R + o_);
;             v0[0] += scale * bflo(r.x); v0[1] += scale * bfhi(r.x); v0[2] += scale * bflo(r.y); v0[3] += scale * bfhi(r.y);
;             v1[0] += scale * bflo(r.z); v1[1] += scale * bfhi(r.z); v1[2] += scale * bflo(r.w); v1[3] += scale * bfhi(r.w);
;             *(u32x4*)(O + o_) = pg8::pack8(v0, v1);
	v_lshlrev_b32_e32 v170, 16, v138
	v_and_b32_e32 v171, 0xffff0000, v138
	v_lshlrev_b32_e32 v172, 16, v139
	v_and_b32_e32 v173, 0xffff0000, v139
	v_lshlrev_b32_e32 v174, 16, v140
	v_and_b32_e32 v175, 0xffff0000, v140
	v_lshlrev_b32_e32 v176, 16, v141
	v_and_b32_e32 v177, 0xffff0000, v141
	v_pk_fma_f32 v[66:67], v[170:171], s[10:11], v[66:67] op_sel_hi:[1,0,1]
	v_pk_fma_f32 v[68:69], v[172:173], s[10:11], v[68:69] op_sel_hi:[1,0,1]
	v_pk_fma_f32 v[62:63], v[174:175], s[10:11], v[62:63] op_sel_hi:[1,0,1]
	v_pk_fma_f32 v[64:65], v[176:177], s[10:11], v[64:65] op_sel_hi:[1,0,1]
	v_cvt_pk_bf16_f32 v138, v66, v67
	v_cvt_pk_bf16_f32 v139, v68, v69
	v_cvt_pk_bf16_f32 v140, v62, v63
	v_cvt_pk_bf16_f32 v141, v64, v65
	v_add_u32_e32 v178, 0x40000, v136
	global_store_dwordx4 v178, v[138:141], s[2:3]
	v_lshlrev_b32_e32 v180, 16, v142
	v_and_b32_e32 v181, 0xffff0000, v142
	v_lshlrev_b32_e32 v182, 16, v143
	v_and_b32_e32 v183, 0xffff0000, v143
	v_lshlrev_b32_e32 v184, 16, v144
	v_and_b32_e32 v185, 0xffff0000, v144
	v_lshlrev_b32_e32 v186, 16, v145
	v_and_b32_e32 v187, 0xffff0000, v145
	v_pk_fma_f32 v[58:59], v[180:181], s[10:11], v[58:59] op_sel_hi:[1,0,1]
	v_pk_fma_f32 v[60:61], v[182:183], s[10:11], v[60:61] op_sel_hi:[1,0,1]
	v_pk_fma_f32 v[54:55], v[184:185], s[10:11], v[54:55] op_sel_hi:[1,0,1]
	v_pk_fma_f32 v[56:57], v[186:187], s[10:11], v[56:57] op_sel_hi:[1,0,1]
	v_cvt_pk_bf16_f32 v142, v58, v59
	v_cvt_pk_bf16_f32 v143, v60, v61
	v_cvt_pk_bf16_f32 v144, v54, v55
	v_cvt_pk_bf16_f32 v145, v56, v57
	v_add_u32_e32 v188, 0x40000, v137
	global_store_dwordx4 v188, v[142:145], s[2:3]
	v_lshlrev_b32_e32 v170, 16, v146
	v_and_b32_e32 v171, 0xffff0000, v146
	v_lshlrev_b32_e32 v172, 16, v147
	v_and_b32_e32 v173, 0xffff0000, v147
	v_lshlrev_b32_e32 v174, 16, v148
	v_and_b32_e32 v175, 0xffff0000, v148
	v_lshlrev_b32_e32 v176, 16, v149
	v_and_b32_e32 v177, 0xffff0000, v149
	v_pk_fma_f32 v[50:51], v[170:171], s[10:11], v[50:51] op_sel_hi:[1,0,1]
	v_pk_fma_f32 v[52:53], v[172:173], s[10:11], v[52:53] op_sel_hi:[1,0,1]
	v_pk_fma_f32 v[46:47], v[174:175], s[10:11], v[46:47] op_sel_hi:[1,0,1]
	v_pk_fma_f32 v[48:49], v[176:177], s[10:11], v[48:49] op_sel_hi:[1,0,1]
	v_cvt_pk_bf16_f32 v146, v50, v51
	v_cvt_pk_bf16_f32 v147, v52, v53
	v_cvt_pk_bf16_f32 v148, v46, v47
	v_cvt_pk_bf16_f32 v149, v48, v49
	v_add_u32_e32 v178, 0x48000, v136
	global_store_dwordx4 v178, v[146:149], s[2:3]
	v_lshlrev_b32_e32 v180, 16, v150
	v_and_b32_e32 v181, 0xffff0000, v150
	v_lshlrev_b32_e32 v182, 16, v151
	v_and_b32_e32 v183, 0xffff0000, v151
	v_lshlrev_b32_e32 v184, 16, v152
	v_and_b32_e32 v185, 0xffff0000, v152
	v_lshlrev_b32_e32 v186, 16, v153
	v_and_b32_e32 v187, 0xffff0000, v153
	v_pk_fma_f32 v[42:43], v[180:181], s[10:11], v[42:43] op_sel_hi:[1,0,1]
	v_pk_fma_f32 v[44:45], v[182:183], s[10:11], v[44:45] op_sel_hi:[1,0,1]
	v_pk_fma_f32 v[38:39], v[184:185], s[10:11], v[38:39] op_sel_hi:[1,0,1]
	v_pk_fma_f32 v[40:41], v[186:187], s[10:11], v[40:41] op_sel_hi:[1,0,1]
	v_cvt_pk_bf16_f32 v150, v42, v43
	v_cvt_pk_bf16_f32 v151, v44, v45
	v_cvt_pk_bf16_f32 v152, v38, v39
	v_cvt_pk_bf16_f32 v153, v40, v41
	v_add_u32_e32 v188, 0x48000, v137
	global_store_dwordx4 v188, v[150:153], s[2:3]
	v_lshlrev_b32_e32 v170, 16, v154
	v_and_b32_e32 v171, 0xffff0000, v154
	v_lshlrev_b32_e32 v172, 16, v155
	v_and_b32_e32 v173, 0xffff0000, v155
	v_lshlrev_b32_e32 v174, 16, v156
	v_and_b32_e32 v175, 0xffff0000, v156
	v_lshlrev_b32_e32 v176, 16, v157
	v_and_b32_e32 v177, 0xffff0000, v157
	v_pk_fma_f32 v[34:35], v[170:171], s[10:11], v[34:35] op_sel_hi:[1,0,1]
	v_pk_fma_f32 v[36:37], v[172:173], s[10:11], v[36:37] op_sel_hi:[1,0,1]
	v_pk_fma_f32 v[30:31], v[174:175], s[10:11], v[30:31] op_sel_hi:[1,0,1]
	v_pk_fma_f32 v[32:33], v[176:177], s[10:11], v[32:33] op_sel_hi:[1,0,1]
	v_cvt_pk_bf16_f32 v154, v34, v35
	v_cvt_pk_bf16_f32 v155, v36, v37
	v_cvt_pk_bf16_f32 v156, v30, v31
	v_cvt_pk_bf16_f32 v157, v32, v33
	v_add_u32_e32 v178, 0x50000, v136
	global_store_dwordx4 v178, v[154:157], s[2:3]
	v_lshlrev_b32_e32 v180, 16, v158
	v_and_b32_e32 v181, 0xffff0000, v158
	v_lshlrev_b32_e32 v182, 16, v159
	v_and_b32_e32 v183, 0xffff0000, v159
	v_lshlrev_b32_e32 v184, 16, v160
	v_and_b32_e32 v185, 0xffff0000, v160
	v_lshlrev_b32_e32 v186, 16, v161
	v_and_b32_e32 v187, 0xffff0000, v161
	v_pk_fma_f32 v[26:27], v[180:181], s[10:11], v[26:27] op_sel_hi:[1,0,1]
	v_pk_fma_f32 v[28:29], v[182:183], s[10:11], v[28:29] op_sel_hi:[1,0,1]
	v_pk_fma_f32 v[22:23], v[184:185], s[10:11], v[22:23] op_sel_hi:[1,0,1]
	v_pk_fma_f32 v[24:25], v[186:187], s[10:11], v[24:25] op_sel_hi:[1,0,1]
	v_cvt_pk_bf16_f32 v158, v26, v27
	v_cvt_pk_bf16_f32 v159, v28, v29
	v_cvt_pk_bf16_f32 v160, v22, v23
	v_cvt_pk_bf16_f32 v161, v24, v25
	v_add_u32_e32 v188, 0x50000, v137
	global_store_dwordx4 v188, v[158:161], s[2:3]
	v_lshlrev_b32_e32 v170, 16, v162
	v_and_b32_e32 v171, 0xffff0000, v162
	v_lshlrev_b32_e32 v172, 16, v163
	v_and_b32_e32 v173, 0xffff0000, v163
	v_lshlrev_b32_e32 v174, 16, v164
	v_and_b32_e32 v175, 0xffff0000, v164
	v_lshlrev_b32_e32 v176, 16, v165
	v_and_b32_e32 v177, 0xffff0000, v165
	v_pk_fma_f32 v[18:19], v[170:171], s[10:11], v[18:19] op_sel_hi:[1,0,1]
	v_pk_fma_f32 v[20:21], v[172:173], s[10:11], v[20:21] op_sel_hi:[1,0,1]
	v_pk_fma_f32 v[14:15], v[174:175], s[10:11], v[14:15] op_sel_hi:[1,0,1]
	v_pk_fma_f32 v[16:17], v[176:177], s[10:11], v[16:17] op_sel_hi:[1,0,1]
	v_cvt_pk_bf16_f32 v162, v18, v19
	v_cvt_pk_bf16_f32 v163, v20, v21
	v_cvt_pk_bf16_f32 v164, v14, v15
	v_cvt_pk_bf16_f32 v165, v16, v17
	v_add_u32_e32 v178, 0x58000, v136
	global_store_dwordx4 v178, v[162:165], s[2:3]
	v_lshlrev_b32_e32 v180, 16, v166
	v_and_b32_e32 v181, 0xffff0000, v166
	v_lshlrev_b32_e32 v182, 16, v167
	v_and_b32_e32 v183, 0xffff0000, v167
	v_lshlrev_b32_e32 v184, 16, v168
	v_and_b32_e32 v185, 0xffff0000, v168
	v_lshlrev_b32_e32 v186, 16, v169
	v_and_b32_e32 v187, 0xffff0000, v169
	v_pk_fma_f32 v[10:11], v[180:181], s[10:11], v[10:11] op_sel_hi:[1,0,1]
	v_pk_fma_f32 v[12:13], v[182:183], s[10:11], v[12:13] op_sel_hi:[1,0,1]
	v_pk_fma_f32 v[6:7], v[184:185], s[10:11], v[6:7] op_sel_hi:[1,0,1]
	v_pk_fma_f32 v[8:9], v[186:187], s[10:11], v[8:9] op_sel_hi:[1,0,1]
	v_cvt_pk_bf16_f32 v166, v10, v11
	v_cvt_pk_bf16_f32 v167, v12, v13
	v_cvt_pk_bf16_f32 v168, v6, v7
	v_cvt_pk_bf16_f32 v169, v8, v9
	v_add_u32_e32 v188, 0x58000, v137
	global_store_dwordx4 v188, v[166:169], s[2:3]
	s_cbranch_vccnz .LBB0_4768
	s_andn2_b64 vcc, exec, s[6:7]
	s_cbranch_vccnz .LBB0_4767
	s_barrier
	s_branch .LBB0_4767
